# attention unit prologue: first key tile's K/V loads issued right after the unit barrier and all 8 Q loads issued up front (renamed into free quads), so the prologue exposes one round trip instead of a
# baseline (speedup 1.0000x reference)
.LBB0_266:
	s_or_b64 exec, exec, s[10:11]
	v_readlane_b32 s4, v254, 33
	s_waitcnt lgkmcnt(0)
	s_barrier
	v_mov_b32_e32 v0, s4
	ds_read_b32 v0, v0
	s_mov_b64 s[10:11], -1
	s_waitcnt lgkmcnt(0)
	v_readfirstlane_b32 s12, v0
	s_cmpk_gt_i32 s12, 0x1ff
	s_cbranch_scc1 .LBB0_261
	v_mov_b32_e32 v3, v178
	s_and_b32 s40, s12, 3
	v_lshlrev_b32_e32 v2, 2, v3
	v_bfe_u32 v4, v3, 5, 1
	v_and_b32_e32 v2, 12, v2
	v_bfe_u32 v5, v3, 2, 2
	v_bitop3_b32 v6, v2, v4, v5 bitop3:0x36
	v_lshlrev_b32_e32 v2, 2, v4
	v_lshrrev_b32_e32 v8, 3, v3
	v_bfe_u32 v9, v3, 1, 1
	v_or_b32_e32 v7, v2, v5
	v_and_or_b32 v8, v8, 2, v9
	v_lshlrev_b32_e32 v5, 2, v5
	v_bitop3_b32 v4, v5, v8, v4 bitop3:0x36
	v_lshlrev_b32_e32 v5, 3, v3
	v_lshlrev_b32_e32 v7, 8, v7
	v_lshlrev_b32_e32 v4, 4, v4
	v_and_b32_e32 v8, 8, v5
	v_or3_b32 v4, v7, v8, v4
	v_add_u32_e32 v4, 0x8000, v4
	v_mov_b32_e32 v9, 0x800
	v_xor_b32_e32 v7, 0x60, v4
	v_and_b32_e32 v0, 31, v3
	v_xad_u32 v16, v4, 32, v9
	v_mov_b32_e32 v17, v4
	v_xor_b32_e32 v18, 64, v4
	v_add_u32_e32 v19, 0x800, v7
	v_xor_b32_e32 v20, 0x80, v4
	v_xor_b32_e32 v7, 0xa0, v4
	v_xor_b32_e32 v22, 0xc0, v4
	v_xor_b32_e32 v4, 0xe0, v4
	v_add_u32_e32 v23, 0x800, v4
	v_lshlrev_b32_e32 v4, 8, v0
	v_add_u32_e32 v21, 0x800, v7
	v_lshl_or_b32 v241, v6, 4, v4
	v_ashrrev_i32_e32 v4, 4, v3
	s_movk_i32 s4, 0x2400
	v_and_b32_e32 v7, 15, v3
	v_mul_lo_u32 v6, v4, s4
	s_lshl_b32 s30, s40, 8
	v_lshlrev_b32_e32 v8, 3, v7
	v_and_b32_e32 v240, 63, v3
	v_or3_b32 v6, v6, v8, s30
	v_ashrrev_i32_e32 v3, 5, v3
	s_bfe_u32 s18, s12, 0x20002
	s_ashr_i32 s12, s12, 4
	v_lshl_add_u32 v214, v6, 1, v9
	v_mul_lo_u32 v6, v3, s4
	v_and_b32_e32 v5, 0xf8, v5
	s_sub_i32 s21, 31, s12
	v_or3_b32 v5, v6, v5, s30
	v_mov_b32_e32 v6, 0x1000
	v_lshl_add_u32 v216, v5, 1, v6
	v_lshlrev_b32_e32 v6, 2, v4
	s_lshl_b32 s41, s18, 12
	s_lshl_b32 s10, s21, 7
	v_and_b32_e32 v6, 12, v6
	v_bfe_u32 v8, v4, 2, 2
	s_add_i32 s10, s10, s41
	v_readlane_b32 s4, v254, 25
	v_lshlrev_b32_e32 v5, 8, v4
	v_bitop3_b32 v6, v6, v7, v8 bitop3:0x36
	s_or_b32 s20, s10, s4
	v_lshl_or_b32 v24, v6, 4, v5
	v_lshlrev_b32_e32 v4, 14, v4
	v_lshlrev_b32_e32 v5, 2, v3
	s_mul_i32 s11, s20, 0x4800
	v_and_b32_e32 v4, 0x4000, v4
	v_and_b32_e32 v5, 12, v5
	v_bfe_u32 v6, v3, 2, 2
	s_mul_hi_u32 s10, s20, 0x4800
	s_add_u32 s11, s8, s11
	v_bitop3_b32 v5, v5, v7, v6 bitop3:0x36
	v_lshl_add_u32 v3, v3, 8, v4
	s_addc_u32 s10, s9, s10
	s_lshl_b32 s42, s40, 9
	v_lshl_or_b32 v3, v5, 4, v3
	s_add_u32 s11, s11, s42
	v_add_u32_e32 v25, 0x8000, v3
	v_mov_b32_e32 v34, v240
	s_addc_u32 s42, s10, 0
	v_readlane_b32 s4, v254, 17
	s_barrier
	v_mov_b32_e32 v212, v178
	s_mul_i32 s100, s18, 0x4800000
	s_add_u32 s100, s8, s100
	s_addc_u32 s101, s9, 0
	v_add_u32_e32 v184, 0x90000, v214
	v_add_u32_e32 v188, 0x90000, v214
	v_add_u32_e32 v192, 0x48000, v216
	v_add_u32_e32 v200, 0x90000, v216
	v_add_u32_e32 v204, 0xd8000, v216
	global_load_dwordx4 v[176:179], v214, s[100:101]
	global_load_dwordx4 v[180:183], v214, s[100:101] offset:256
	global_load_dwordx4 v[184:187], v184, s[100:101]
	global_load_dwordx4 v[188:191], v188, s[100:101] offset:256
	global_load_dwordx4 v[192:195], v192, s[100:101]
	global_load_dwordx4 v[200:203], v200, s[100:101]
	global_load_dwordx4 v[196:199], v216, s[100:101]
	global_load_dwordx4 v[204:207], v204, s[100:101]
	s_add_u32 s10, s11, s4
	v_and_b32_e32 v3, 15, v34
	v_ashrrev_i32_e32 v32, 4, v34
	s_movk_i32 s4, 0x4800
	v_lshlrev_b32_e32 v35, 4, v3
	v_mul_lo_u32 v4, v32, s4
	s_addc_u32 s11, s42, 0
	v_or_b32_e32 v4, v4, v35
	v_add_u32_e32 v48, 0x12000, v4
	v_add_u32_e32 v52, 0x24000, v4
	v_add_u32_e32 v56, 0x36000, v4
	v_add_u32_e32 v60, 0x48000, v4
	v_add_u32_e32 v64, 0x5a000, v4
	v_add_u32_e32 v68, 0x6c000, v4
	v_add_u32_e32 v72, 0x7e000, v4
	global_load_dwordx4 v[44:47], v4, s[10:11]
	global_load_dwordx4 v[48:51], v48, s[10:11]
	global_load_dwordx4 v[52:55], v52, s[10:11]
	global_load_dwordx4 v[56:59], v56, s[10:11]
	global_load_dwordx4 v[60:63], v60, s[10:11]
	global_load_dwordx4 v[64:67], v64, s[10:11]
	global_load_dwordx4 v[68:71], v68, s[10:11]
	global_load_dwordx4 v[72:75], v72, s[10:11]
	v_add_u32_e32 v8, 64, v34
	v_ashrrev_i32_e32 v33, 4, v8
	v_mul_lo_u32 v8, v33, s4
	v_or_b32_e32 v8, v8, v35
	v_add_u32_e32 v12, 0x80, v34
	v_ashrrev_i32_e32 v36, 4, v12
	v_mul_lo_u32 v12, v36, s4
	v_or_b32_e32 v12, v12, v35
	s_mov_b32 s6, 0x3e0293ee
	v_lshlrev_b32_e32 v39, 8, v33
	s_lshl_b32 s70, s21, 1
	s_add_i32 s21, s70, 2
	s_mul_i32 s18, s18, 0x4800000
	v_mov_b32_e32 v215, v1
	v_mov_b32_e32 v217, v1
	s_mov_b32 s5, 0x48000
	v_add_u32_e32 v250, 0, v24
	v_add_u32_e32 v251, 0, v25
	v_add_u32_e32 v228, 0, v17
	v_add_u32_e32 v230, 0, v16
	v_add_u32_e32 v237, 0, v18
	v_add_u32_e32 v233, 0, v19
	v_add_u32_e32 v238, 0, v20
	v_add_u32_e32 v232, 0, v21
	v_add_u32_e32 v236, 0, v22
	v_add_u32_e32 v224, 0, v23
	v_mov_b32_e32 v226, 0x41b17218
	v_xor_b32_e32 v242, 32, v241
	v_xor_b32_e32 v243, 64, v241
	v_xor_b32_e32 v244, 0x60, v241
	v_xor_b32_e32 v245, 0x80, v241
	v_xor_b32_e32 v246, 0xa0, v241
	v_xor_b32_e32 v247, 0xc0, v241
	v_xor_b32_e32 v248, 0xe0, v241
	v_mov_b32_e32 v208, 0
	s_waitcnt vmcnt(7)
	v_lshlrev_b32_e32 v26, 16, v44
	v_and_b32_e32 v27, 0xffff0000, v44
	v_pk_mul_f32 v[26:27], v[26:27], s[6:7] op_sel_hi:[1,0]
	v_lshlrev_b32_e32 v30, 16, v46
	v_cvt_pk_bf16_f32 v4, v26, v27
	v_lshlrev_b32_e32 v26, 16, v45
	v_and_b32_e32 v27, 0xffff0000, v45
	v_pk_mul_f32 v[26:27], v[26:27], s[6:7] op_sel_hi:[1,0]
	v_and_b32_e32 v31, 0xffff0000, v46
	v_cvt_pk_bf16_f32 v5, v26, v27
	v_add_u32_e32 v26, 0xc0, v34
	v_pk_mul_f32 v[30:31], v[30:31], s[6:7] op_sel_hi:[1,0]
	v_ashrrev_i32_e32 v37, 4, v26
	v_cvt_pk_bf16_f32 v6, v30, v31
	v_lshlrev_b32_e32 v30, 16, v47
	v_and_b32_e32 v31, 0xffff0000, v47
	v_mul_lo_u32 v26, v37, s4
	v_pk_mul_f32 v[30:31], v[30:31], s[6:7] op_sel_hi:[1,0]
	v_or_b32_e32 v26, v26, v35
	v_cvt_pk_bf16_f32 v7, v30, v31
	v_lshlrev_b32_e32 v31, 2, v32
	v_lshlrev_b32_e32 v30, 8, v32
	v_and_b32_e32 v31, 12, v31
	v_bfe_u32 v32, v32, 2, 2
	v_bitop3_b32 v31, v31, v3, v32 bitop3:0x36
	v_lshlrev_b32_e32 v31, 4, v31
	v_add3_u32 v30, s17, v31, v30
	ds_write_b128 v30, v[4:7]
	s_waitcnt vmcnt(6)
	v_lshlrev_b32_e32 v4, 16, v48
	v_and_b32_e32 v5, 0xffff0000, v48
	v_pk_mul_f32 v[30:31], v[4:5], s[6:7] op_sel_hi:[1,0]
	v_add_u32_e32 v4, 0x100, v34
	v_ashrrev_i32_e32 v38, 4, v4
	v_mul_lo_u32 v4, v38, s4
	v_or_b32_e32 v4, v4, v35
	v_cvt_pk_bf16_f32 v8, v30, v31
	v_lshlrev_b32_e32 v30, 16, v49
	v_and_b32_e32 v31, 0xffff0000, v49
	v_pk_mul_f32 v[30:31], v[30:31], s[6:7] op_sel_hi:[1,0]
	s_nop 0
	v_cvt_pk_bf16_f32 v9, v30, v31
	v_lshlrev_b32_e32 v30, 16, v50
	v_and_b32_e32 v31, 0xffff0000, v50
	v_pk_mul_f32 v[30:31], v[30:31], s[6:7] op_sel_hi:[1,0]
	s_nop 0
	v_cvt_pk_bf16_f32 v10, v30, v31
	v_lshlrev_b32_e32 v30, 16, v51
	v_and_b32_e32 v31, 0xffff0000, v51
	v_pk_mul_f32 v[30:31], v[30:31], s[6:7] op_sel_hi:[1,0]
	s_nop 0
	v_cvt_pk_bf16_f32 v11, v30, v31
	v_lshlrev_b32_e32 v30, 2, v33
	v_and_b32_e32 v30, 12, v30
	v_bfe_u32 v31, v33, 2, 2
	v_bitop3_b32 v30, v30, v3, v31 bitop3:0x36
	v_lshlrev_b32_e32 v40, 4, v30
	v_add_u32_e32 v30, 0x140, v34
	v_ashrrev_i32_e32 v41, 4, v30
	v_mul_lo_u32 v30, v41, s4
	v_or_b32_e32 v30, v30, v35
	v_add3_u32 v39, s17, v40, v39
	ds_write_b128 v39, v[8:11]
	s_waitcnt vmcnt(5)
	v_lshlrev_b32_e32 v8, 16, v52
	v_and_b32_e32 v9, 0xffff0000, v52
	v_lshlrev_b32_e32 v10, 16, v53
	v_and_b32_e32 v11, 0xffff0000, v53
	v_pk_mul_f32 v[8:9], v[8:9], s[6:7] op_sel_hi:[1,0]
	v_pk_mul_f32 v[10:11], v[10:11], s[6:7] op_sel_hi:[1,0]
	v_cvt_pk_bf16_f32 v8, v8, v9
	v_cvt_pk_bf16_f32 v9, v10, v11
	v_lshlrev_b32_e32 v10, 16, v54
	v_and_b32_e32 v11, 0xffff0000, v54
	v_lshlrev_b32_e32 v12, 16, v55
	v_and_b32_e32 v13, 0xffff0000, v55
	v_pk_mul_f32 v[10:11], v[10:11], s[6:7] op_sel_hi:[1,0]
	v_pk_mul_f32 v[12:13], v[12:13], s[6:7] op_sel_hi:[1,0]
	v_cvt_pk_bf16_f32 v10, v10, v11
	v_cvt_pk_bf16_f32 v11, v12, v13
	v_lshlrev_b32_e32 v12, 2, v36
	v_and_b32_e32 v12, 12, v12
	v_bfe_u32 v13, v36, 2, 2
	v_bitop3_b32 v12, v12, v3, v13 bitop3:0x36
	v_lshlrev_b32_e32 v39, 8, v36
	v_lshlrev_b32_e32 v36, 4, v12
	v_add_u32_e32 v12, 0x180, v34
	v_ashrrev_i32_e32 v40, 4, v12
	v_mul_lo_u32 v12, v40, s4
	v_or_b32_e32 v12, v12, v35
	v_add3_u32 v36, s17, v36, v39
	ds_write_b128 v36, v[8:11]
	s_waitcnt vmcnt(4)
	v_lshlrev_b32_e32 v8, 16, v56
	v_and_b32_e32 v9, 0xffff0000, v56
	v_lshlrev_b32_e32 v10, 16, v57
	v_and_b32_e32 v11, 0xffff0000, v57
	v_pk_mul_f32 v[8:9], v[8:9], s[6:7] op_sel_hi:[1,0]
	v_pk_mul_f32 v[10:11], v[10:11], s[6:7] op_sel_hi:[1,0]
	v_cvt_pk_bf16_f32 v8, v8, v9
	v_cvt_pk_bf16_f32 v9, v10, v11
	v_lshlrev_b32_e32 v10, 16, v58
	v_and_b32_e32 v11, 0xffff0000, v58
	v_lshlrev_b32_e32 v26, 16, v59
	v_and_b32_e32 v27, 0xffff0000, v59
	v_pk_mul_f32 v[10:11], v[10:11], s[6:7] op_sel_hi:[1,0]
	v_pk_mul_f32 v[26:27], v[26:27], s[6:7] op_sel_hi:[1,0]
	v_cvt_pk_bf16_f32 v10, v10, v11
	v_cvt_pk_bf16_f32 v11, v26, v27
	v_lshlrev_b32_e32 v27, 2, v37
	v_and_b32_e32 v27, 12, v27
	v_bfe_u32 v28, v37, 2, 2
	v_bitop3_b32 v27, v27, v3, v28 bitop3:0x36
	v_lshlrev_b32_e32 v26, 8, v37
	v_lshlrev_b32_e32 v27, 4, v27
	v_add3_u32 v26, s17, v27, v26
	ds_write_b128 v26, v[8:11]
	s_waitcnt vmcnt(3)
	v_lshlrev_b32_e32 v8, 16, v60
	v_and_b32_e32 v9, 0xffff0000, v60
	v_pk_mul_f32 v[8:9], v[8:9], s[6:7] op_sel_hi:[1,0]
	v_bfe_u32 v10, v38, 2, 2
	v_cvt_pk_bf16_f32 v4, v8, v9
	v_lshlrev_b32_e32 v8, 16, v61
	v_and_b32_e32 v9, 0xffff0000, v61
	v_pk_mul_f32 v[8:9], v[8:9], s[6:7] op_sel_hi:[1,0]
	v_bfe_u32 v29, v41, 2, 2
	v_cvt_pk_bf16_f32 v5, v8, v9
	v_lshlrev_b32_e32 v8, 16, v62
	v_and_b32_e32 v9, 0xffff0000, v62
	v_pk_mul_f32 v[8:9], v[8:9], s[6:7] op_sel_hi:[1,0]
	s_waitcnt vmcnt(2)
	v_lshlrev_b32_e32 v26, 16, v67
	v_cvt_pk_bf16_f32 v6, v8, v9
	v_lshlrev_b32_e32 v8, 16, v63
	v_and_b32_e32 v9, 0xffff0000, v63
	v_pk_mul_f32 v[8:9], v[8:9], s[6:7] op_sel_hi:[1,0]
	v_and_b32_e32 v27, 0xffff0000, v67
	v_cvt_pk_bf16_f32 v7, v8, v9
	v_lshlrev_b32_e32 v9, 2, v38
	v_and_b32_e32 v9, 12, v9
	v_bitop3_b32 v9, v9, v3, v10 bitop3:0x36
	v_lshlrev_b32_e32 v8, 8, v38
	v_lshlrev_b32_e32 v9, 4, v9
	v_add3_u32 v8, s17, v9, v8
	ds_write_b128 v8, v[4:7]
	v_lshlrev_b32_e32 v4, 16, v64
	v_and_b32_e32 v5, 0xffff0000, v64
	v_pk_mul_f32 v[4:5], v[4:5], s[6:7] op_sel_hi:[1,0]
	v_lshlrev_b32_e32 v6, 16, v65
	v_cvt_pk_bf16_f32 v4, v4, v5
	v_add_u32_e32 v5, 0x1c0, v34
	v_ashrrev_i32_e32 v28, 4, v5
	v_mul_lo_u32 v5, v28, s4
	v_and_b32_e32 v7, 0xffff0000, v65
	v_or_b32_e32 v5, v5, v35
	v_pk_mul_f32 v[6:7], v[6:7], s[6:7] op_sel_hi:[1,0]
	v_cvt_pk_bf16_f32 v5, v6, v7
	v_lshlrev_b32_e32 v6, 16, v66
	v_and_b32_e32 v7, 0xffff0000, v66
	v_pk_mul_f32 v[6:7], v[6:7], s[6:7] op_sel_hi:[1,0]
	v_pk_mul_f32 v[26:27], v[26:27], s[6:7] op_sel_hi:[1,0]
	v_cvt_pk_bf16_f32 v6, v6, v7
	v_cvt_pk_bf16_f32 v7, v26, v27
	v_lshlrev_b32_e32 v27, 2, v41
	v_and_b32_e32 v27, 12, v27
	v_bitop3_b32 v27, v27, v3, v29 bitop3:0x36
	v_lshlrev_b32_e32 v26, 8, v41
	v_lshlrev_b32_e32 v27, 4, v27
	v_add3_u32 v26, s17, v27, v26
	ds_write_b128 v26, v[4:7]
	s_waitcnt vmcnt(1)
	v_lshlrev_b32_e32 v4, 16, v68
	v_and_b32_e32 v5, 0xffff0000, v68
	v_lshlrev_b32_e32 v6, 16, v69
	v_and_b32_e32 v7, 0xffff0000, v69
	v_pk_mul_f32 v[4:5], v[4:5], s[6:7] op_sel_hi:[1,0]
	v_pk_mul_f32 v[6:7], v[6:7], s[6:7] op_sel_hi:[1,0]
	v_cvt_pk_bf16_f32 v4, v4, v5
	v_cvt_pk_bf16_f32 v5, v6, v7
	v_lshlrev_b32_e32 v6, 16, v70
	v_and_b32_e32 v7, 0xffff0000, v70
	v_lshlrev_b32_e32 v12, 16, v71
	v_and_b32_e32 v13, 0xffff0000, v71
	v_pk_mul_f32 v[6:7], v[6:7], s[6:7] op_sel_hi:[1,0]
	v_pk_mul_f32 v[12:13], v[12:13], s[6:7] op_sel_hi:[1,0]
	v_cvt_pk_bf16_f32 v6, v6, v7
	v_cvt_pk_bf16_f32 v7, v12, v13
	v_lshlrev_b32_e32 v13, 2, v40
	v_and_b32_e32 v13, 12, v13
	v_bfe_u32 v14, v40, 2, 2
	s_not_b32 s10, s40
	v_bitop3_b32 v13, v13, v3, v14 bitop3:0x36
	s_lshl_b32 s40, s10, 1
	v_lshlrev_b32_e32 v12, 8, v40
	v_lshlrev_b32_e32 v13, 4, v13
	s_add_u32 s10, s8, s18
	v_add3_u32 v12, s17, v13, v12
	s_addc_u32 s11, s9, 0
	ds_write_b128 v12, v[4:7]
	s_mov_b32 s4, 0x90000
	s_mov_b32 s18, 0xd8000
	s_nop 0
	v_readlane_b32 s4, v254, 26
	s_nop 0
	s_lshl_b32 s10, s12, 7
	s_add_i32 s10, s4, s10
	v_add_u32_e32 v2, s10, v2
	v_mov_b32_e32 v14, v1
	v_mov_b32_e32 v15, v1
	v_sub_u32_e32 v249, v2, v0
	v_mov_b32_e32 v0, v1
	v_mov_b32_e32 v2, v1
	v_mov_b32_e32 v12, v1
	v_mov_b32_e32 v13, v1
	s_or_b32 s18, s41, 64
	s_waitcnt vmcnt(0)
	v_lshlrev_b32_e32 v4, 16, v72
	v_and_b32_e32 v5, 0xffff0000, v72
	v_lshlrev_b32_e32 v6, 16, v73
	v_and_b32_e32 v7, 0xffff0000, v73
	v_pk_mul_f32 v[4:5], v[4:5], s[6:7] op_sel_hi:[1,0]
	v_pk_mul_f32 v[6:7], v[6:7], s[6:7] op_sel_hi:[1,0]
	v_cvt_pk_bf16_f32 v4, v4, v5
	v_cvt_pk_bf16_f32 v5, v6, v7
	v_lshlrev_b32_e32 v6, 16, v74
	v_and_b32_e32 v7, 0xffff0000, v74
	v_lshlrev_b32_e32 v8, 16, v75
	v_and_b32_e32 v9, 0xffff0000, v75
	v_cvt_f32_i32_e32 v10, s40
	v_pk_mul_f32 v[6:7], v[6:7], s[6:7] op_sel_hi:[1,0]
	v_pk_mul_f32 v[8:9], v[8:9], s[6:7] op_sel_hi:[1,0]
	v_cvt_pk_bf16_f32 v6, v6, v7
	v_cvt_pk_bf16_f32 v7, v8, v9
	v_lshlrev_b32_e32 v9, 2, v28
	v_and_b32_e32 v9, 12, v9
	v_bfe_u32 v11, v28, 2, 2
	v_bitop3_b32 v3, v9, v3, v11 bitop3:0x36
	v_exp_f32_e32 v9, v10
	v_lshlrev_b32_e32 v8, 8, v28
	v_lshlrev_b32_e32 v3, 4, v3
	v_add3_u32 v3, s17, v3, v8
	ds_write_b128 v3, v[4:7]
	v_mul_f32_e32 v218, 0x3fb8aa3b, v9
	v_mov_b32_e32 v3, v1
	v_mov_b32_e32 v4, v1
	v_mov_b32_e32 v5, v1
	v_mov_b32_e32 v6, v1
	v_mov_b32_e32 v7, v1
	v_mov_b32_e32 v8, v1
	v_mov_b32_e32 v9, v1
	v_mov_b32_e32 v10, v1
	v_mov_b32_e32 v11, v1
	v_mov_b64_e32 v[30:31], v[14:15]
	v_mov_b64_e32 v[46:47], v[14:15]
	v_mov_b64_e32 v[62:63], v[14:15]
	v_mov_b64_e32 v[78:79], v[14:15]
	v_mov_b64_e32 v[94:95], v[14:15]
	v_mov_b64_e32 v[110:111], v[14:15]
	v_mov_b64_e32 v[126:127], v[14:15]
	v_mov_b64_e32 v[142:143], v[14:15]
	s_mov_b32 s40, 0
	v_mov_b32_e32 v220, v218
	v_mov_b32_e32 v221, v218
	v_mov_b32_e32 v222, v218
	v_mov_b32_e32 v223, v218
	v_mov_b64_e32 v[28:29], v[12:13]
	v_mov_b64_e32 v[26:27], v[10:11]
	v_mov_b64_e32 v[24:25], v[8:9]
	v_mov_b64_e32 v[22:23], v[6:7]
	v_mov_b64_e32 v[20:21], v[4:5]
	v_mov_b64_e32 v[18:19], v[2:3]
	v_mov_b64_e32 v[16:17], v[0:1]
	v_mov_b64_e32 v[44:45], v[12:13]
	v_mov_b64_e32 v[42:43], v[10:11]
	v_mov_b64_e32 v[40:41], v[8:9]
	v_mov_b64_e32 v[38:39], v[6:7]
	v_mov_b64_e32 v[36:37], v[4:5]
	v_mov_b64_e32 v[34:35], v[2:3]
	v_mov_b64_e32 v[32:33], v[0:1]
	v_mov_b64_e32 v[60:61], v[12:13]
	v_mov_b64_e32 v[58:59], v[10:11]
	v_mov_b64_e32 v[56:57], v[8:9]
	v_mov_b64_e32 v[54:55], v[6:7]
	v_mov_b64_e32 v[52:53], v[4:5]
	v_mov_b64_e32 v[50:51], v[2:3]
	v_mov_b64_e32 v[48:49], v[0:1]
	v_mov_b64_e32 v[76:77], v[12:13]
	v_mov_b64_e32 v[74:75], v[10:11]
	v_mov_b64_e32 v[72:73], v[8:9]
	v_mov_b64_e32 v[70:71], v[6:7]
	v_mov_b64_e32 v[68:69], v[4:5]
	v_mov_b64_e32 v[66:67], v[2:3]
	v_mov_b64_e32 v[64:65], v[0:1]
	v_mov_b64_e32 v[92:93], v[12:13]
	v_mov_b64_e32 v[90:91], v[10:11]
	v_mov_b64_e32 v[88:89], v[8:9]
	v_mov_b64_e32 v[86:87], v[6:7]
	v_mov_b64_e32 v[84:85], v[4:5]
	v_mov_b64_e32 v[82:83], v[2:3]
	v_mov_b64_e32 v[80:81], v[0:1]
	v_mov_b64_e32 v[108:109], v[12:13]
	v_mov_b64_e32 v[106:107], v[10:11]
	v_mov_b64_e32 v[104:105], v[8:9]
	v_mov_b64_e32 v[102:103], v[6:7]
	v_mov_b64_e32 v[100:101], v[4:5]
	v_mov_b64_e32 v[98:99], v[2:3]
	v_mov_b64_e32 v[96:97], v[0:1]
	v_mov_b64_e32 v[124:125], v[12:13]
	v_mov_b64_e32 v[122:123], v[10:11]
	v_mov_b64_e32 v[120:121], v[8:9]
	v_mov_b64_e32 v[118:119], v[6:7]
	v_mov_b64_e32 v[116:117], v[4:5]
	v_mov_b64_e32 v[114:115], v[2:3]
	v_mov_b64_e32 v[112:113], v[0:1]
	v_mov_b64_e32 v[140:141], v[12:13]
	v_mov_b64_e32 v[138:139], v[10:11]
	v_mov_b64_e32 v[136:137], v[8:9]
	v_mov_b64_e32 v[134:135], v[6:7]
	v_mov_b64_e32 v[132:133], v[4:5]
	v_mov_b64_e32 v[130:131], v[2:3]
	v_mov_b64_e32 v[128:129], v[0:1]
	v_mov_b32_e32 v15, 0
	s_branch .LBB0_270
